# peel+nt with the four GEMM K-loop heads aligned to 64 bytes (code placement)
# speedup vs baseline: 1.0039x; 1.0005x over previous
.LBB0_310:
	s_ashr_i32 s91, s90, 31
	s_lshl_b64 s[4:5], s[90:91], 20
	s_add_u32 s62, s66, s4
	s_addc_u32 s63, s67, s5
	s_and_b64 s[4:5], s[36:37], exec
	s_cselect_b32 s4, s63, s25
	s_cselect_b32 s5, s62, s24
	s_ashr_i32 s89, s88, 31
	s_lshl_b64 s[20:21], s[88:89], 20
	s_add_u32 s20, s72, s20
	s_addc_u32 s21, s73, s21
	s_and_b64 s[30:31], s[36:37], exec
	s_cselect_b32 s8, s21, s1
	s_cselect_b32 s13, s20, s0
	s_add_u32 s17, s0, 0x10000
	s_addc_u32 s19, s1, 0
	s_add_u32 s0, s24, 0x80080
	s_addc_u32 s1, s25, 0
	s_mov_b32 s28, -2
	v_add_u32_e32 v100, s3, v190
	v_add_u32_e32 v156, s75, v190
	ds_read_b128 v[40:43], v100
	ds_read_b128 v[60:63], v100 offset:1024
	ds_read_b128 v[80:83], v100 offset:2048
	ds_read_b128 v[100:103], v100 offset:3072
	ds_read_b128 v[120:123], v156
	ds_read_b128 v[140:143], v156 offset:1024
	ds_read_b128 v[152:155], v156 offset:2048
	ds_read_b128 v[156:159], v156 offset:3072
	s_add_u32 s24, s0, 0xfff80080
	s_addc_u32 s25, s1, -1
	s_cmp_eq_u32 s28, 28
	s_cselect_b32 s39, s4, s25
	s_cselect_b32 s38, s5, s24
	s_cselect_b32 s25, s8, s19
	s_cselect_b32 s24, s13, s17
	v_lshl_add_u64 v[188:189], s[0:1], 0, v[168:169]
	s_add_i32 m0, s78, 0xc000
	ds_read_b128 v[172:175], v191
	ds_read_b128 v[176:179], v191 offset:1024
	ds_read_b128 v[180:183], v191 offset:2048
	ds_read_b128 v[184:187], v191 offset:3072
	ds_read_b128 v[192:195], v191 offset:4096
	ds_read_b128 v[196:199], v191 offset:5120
	ds_read_b128 v[200:203], v191 offset:6144
	ds_read_b128 v[204:207], v191 offset:7168
	global_load_lds_dwordx4 v[188:189], off
	v_lshl_add_u64 v[188:189], s[0:1], 0, v[170:171]
	s_add_i32 m0, s78, 0xe000
	s_nop 0
	global_load_lds_dwordx4 v[188:189], off
	s_waitcnt vmcnt(8)
	s_waitcnt lgkmcnt(0)
	s_barrier
	s_setprio 1
	s_waitcnt lgkmcnt(0)
	v_mfma_f32_16x16x32_bf16 v[148:151], v[40:43], v[172:175], 0
	v_mfma_f32_16x16x32_bf16 v[144:147], v[80:83], v[172:175], 0
	v_mfma_f32_16x16x32_bf16 v[128:131], v[40:43], v[180:183], 0
	v_mfma_f32_16x16x32_bf16 v[124:127], v[80:83], v[180:183], 0
	v_mfma_f32_16x16x32_bf16 v[108:111], v[40:43], v[192:195], 0
	v_mfma_f32_16x16x32_bf16 v[104:107], v[80:83], v[192:195], 0
	v_mfma_f32_16x16x32_bf16 v[88:91], v[40:43], v[200:203], 0
	v_mfma_f32_16x16x32_bf16 v[84:87], v[80:83], v[200:203], 0
	v_mfma_f32_16x16x32_bf16 v[148:151], v[60:63], v[176:179], v[148:151]
	v_mfma_f32_16x16x32_bf16 v[144:147], v[100:103], v[176:179], v[144:147]
	v_mfma_f32_16x16x32_bf16 v[128:131], v[60:63], v[184:187], v[128:131]
	v_mfma_f32_16x16x32_bf16 v[124:127], v[100:103], v[184:187], v[124:127]
	v_mfma_f32_16x16x32_bf16 v[108:111], v[60:63], v[196:199], v[108:111]
	v_mfma_f32_16x16x32_bf16 v[104:107], v[100:103], v[196:199], v[104:107]
	v_mfma_f32_16x16x32_bf16 v[88:91], v[60:63], v[204:207], v[88:91]
	v_mfma_f32_16x16x32_bf16 v[84:87], v[100:103], v[204:207], v[84:87]
	s_setprio 0
	s_setprio 1
	v_mfma_f32_16x16x32_bf16 v[136:139], v[120:123], v[172:175], 0
	v_mfma_f32_16x16x32_bf16 v[132:135], v[152:155], v[172:175], 0
	v_mfma_f32_16x16x32_bf16 v[116:119], v[120:123], v[180:183], 0
	v_mfma_f32_16x16x32_bf16 v[112:115], v[152:155], v[180:183], 0
	v_mfma_f32_16x16x32_bf16 v[96:99], v[120:123], v[192:195], 0
	v_mfma_f32_16x16x32_bf16 v[92:95], v[152:155], v[192:195], 0
	v_mfma_f32_16x16x32_bf16 v[76:79], v[120:123], v[200:203], 0
	v_mfma_f32_16x16x32_bf16 v[72:75], v[152:155], v[200:203], 0
	v_mfma_f32_16x16x32_bf16 v[136:139], v[140:143], v[176:179], v[136:139]
	v_mfma_f32_16x16x32_bf16 v[132:135], v[156:159], v[176:179], v[132:135]
	v_mfma_f32_16x16x32_bf16 v[116:119], v[140:143], v[184:187], v[116:119]
	v_mfma_f32_16x16x32_bf16 v[112:115], v[156:159], v[184:187], v[112:115]
	v_mfma_f32_16x16x32_bf16 v[96:99], v[140:143], v[196:199], v[96:99]
	v_mfma_f32_16x16x32_bf16 v[92:95], v[156:159], v[196:199], v[92:95]
	v_mfma_f32_16x16x32_bf16 v[76:79], v[140:143], v[204:207], v[76:79]
	v_mfma_f32_16x16x32_bf16 v[72:75], v[156:159], v[204:207], v[72:75]
	s_setprio 0
	s_barrier
	s_mov_b32 m0, s23
	v_lshl_add_u64 v[188:189], s[24:25], 0, v[162:163]
	s_add_u32 s30, s24, 0x4000
	ds_read_b128 v[172:175], v191 offset:16384
	ds_read_b128 v[176:179], v191 offset:17408
	ds_read_b128 v[180:183], v191 offset:18432
	ds_read_b128 v[184:187], v191 offset:19456
	ds_read_b128 v[192:195], v191 offset:20480
	ds_read_b128 v[196:199], v191 offset:21504
	ds_read_b128 v[200:203], v191 offset:22528
	ds_read_b128 v[204:207], v191 offset:23552
	global_load_lds_dwordx4 v[188:189], off
	v_lshl_add_u64 v[188:189], s[24:25], 0, v[166:167]
	s_mov_b32 m0, s74
	s_addc_u32 s31, s25, 0
	global_load_lds_dwordx4 v[188:189], off
	v_lshl_add_u64 v[188:189], s[30:31], 0, v[162:163]
	s_mov_b32 m0, s76
	v_lshl_add_u64 v[208:209], s[38:39], 0, v[164:165]
	global_load_lds_dwordx4 v[188:189], off
	v_lshl_add_u64 v[188:189], s[30:31], 0, v[166:167]
	s_mov_b32 m0, s77
	s_nop 0
	global_load_lds_dwordx4 v[188:189], off
	v_lshl_add_u64 v[188:189], s[38:39], 0, v[160:161]
	s_mov_b32 m0, s78
	s_nop 0
	global_load_lds_dwordx4 v[188:189], off
	s_mov_b32 m0, s79
	s_nop 0
	global_load_lds_dwordx4 v[208:209], off
	s_waitcnt vmcnt(8)
	s_waitcnt lgkmcnt(0)
	s_barrier
	s_setprio 1
	s_waitcnt lgkmcnt(0)
	v_mfma_f32_16x16x32_bf16 v[68:71], v[40:43], v[172:175], 0
	v_mfma_f32_16x16x32_bf16 v[64:67], v[80:83], v[172:175], 0
	v_mfma_f32_16x16x32_bf16 v[48:51], v[40:43], v[180:183], 0
	v_mfma_f32_16x16x32_bf16 v[44:47], v[80:83], v[180:183], 0
	v_mfma_f32_16x16x32_bf16 v[28:31], v[40:43], v[192:195], 0
	v_mfma_f32_16x16x32_bf16 v[24:27], v[80:83], v[192:195], 0
	v_mfma_f32_16x16x32_bf16 v[12:15], v[40:43], v[200:203], 0
	v_mfma_f32_16x16x32_bf16 v[8:11], v[80:83], v[200:203], 0
	v_mfma_f32_16x16x32_bf16 v[68:71], v[60:63], v[176:179], v[68:71]
	v_mfma_f32_16x16x32_bf16 v[64:67], v[100:103], v[176:179], v[64:67]
	v_mfma_f32_16x16x32_bf16 v[48:51], v[60:63], v[184:187], v[48:51]
	v_mfma_f32_16x16x32_bf16 v[44:47], v[100:103], v[184:187], v[44:47]
	v_mfma_f32_16x16x32_bf16 v[28:31], v[60:63], v[196:199], v[28:31]
	v_mfma_f32_16x16x32_bf16 v[24:27], v[100:103], v[196:199], v[24:27]
	v_mfma_f32_16x16x32_bf16 v[12:15], v[60:63], v[204:207], v[12:15]
	v_mfma_f32_16x16x32_bf16 v[8:11], v[100:103], v[204:207], v[8:11]
	s_setprio 0
	s_setprio 1
	v_mfma_f32_16x16x32_bf16 v[52:55], v[152:155], v[172:175], 0
	v_mfma_f32_16x16x32_bf16 v[36:39], v[120:123], v[180:183], 0
	v_mfma_f32_16x16x32_bf16 v[32:35], v[152:155], v[180:183], 0
	v_mfma_f32_16x16x32_bf16 v[20:23], v[120:123], v[192:195], 0
	v_mfma_f32_16x16x32_bf16 v[16:19], v[152:155], v[192:195], 0
	v_mfma_f32_16x16x32_bf16 v[4:7], v[120:123], v[200:203], 0
	v_mfma_f32_16x16x32_bf16 v[0:3], v[152:155], v[200:203], 0
	v_mfma_f32_16x16x32_bf16 v[40:43], v[120:123], v[172:175], 0
	v_mfma_f32_16x16x32_bf16 v[52:55], v[156:159], v[176:179], v[52:55]
	v_mfma_f32_16x16x32_bf16 v[36:39], v[140:143], v[184:187], v[36:39]
	v_mfma_f32_16x16x32_bf16 v[32:35], v[156:159], v[184:187], v[32:35]
	v_mfma_f32_16x16x32_bf16 v[20:23], v[140:143], v[196:199], v[20:23]
	v_mfma_f32_16x16x32_bf16 v[16:19], v[156:159], v[196:199], v[16:19]
	v_mfma_f32_16x16x32_bf16 v[4:7], v[140:143], v[204:207], v[4:7]
	v_mfma_f32_16x16x32_bf16 v[0:3], v[156:159], v[204:207], v[0:3]
	v_mfma_f32_16x16x32_bf16 v[40:43], v[140:143], v[176:179], v[40:43]
	s_setprio 0
	s_barrier
	v_add_u32_e32 v100, s86, v190
	v_add_u32_e32 v156, s95, v190
	ds_read_b128 v[56:59], v100
	ds_read_b128 v[60:63], v100 offset:1024
	ds_read_b128 v[80:83], v100 offset:2048
	ds_read_b128 v[100:103], v100 offset:3072
	ds_read_b128 v[120:123], v156
	ds_read_b128 v[140:143], v156 offset:1024
	ds_read_b128 v[152:155], v156 offset:2048
	ds_read_b128 v[156:159], v156 offset:3072
	s_add_u32 s30, s38, 0x80000
	s_addc_u32 s31, s39, 0
	s_mov_b32 m0, s82
	v_lshl_add_u64 v[210:211], s[30:31], 0, v[160:161]
	ds_read_b128 v[172:175], v191 offset:32768
	ds_read_b128 v[176:179], v191 offset:33792
	ds_read_b128 v[180:183], v191 offset:34816
	ds_read_b128 v[184:187], v191 offset:35840
	ds_read_b128 v[192:195], v191 offset:36864
	ds_read_b128 v[196:199], v191 offset:37888
	ds_read_b128 v[200:203], v191 offset:38912
	ds_read_b128 v[204:207], v191 offset:39936
	global_load_lds_dwordx4 v[210:211], off
	v_lshl_add_u64 v[210:211], s[30:31], 0, v[164:165]
	s_mov_b32 m0, s83
	s_nop 0
	global_load_lds_dwordx4 v[210:211], off
	s_waitcnt vmcnt(8)
	s_waitcnt lgkmcnt(0)
	s_barrier
	s_setprio 1
	s_waitcnt lgkmcnt(0)
	v_mfma_f32_16x16x32_bf16 v[148:151], v[56:59], v[172:175], v[148:151]
	v_mfma_f32_16x16x32_bf16 v[144:147], v[80:83], v[172:175], v[144:147]
	v_mfma_f32_16x16x32_bf16 v[128:131], v[56:59], v[180:183], v[128:131]
	v_mfma_f32_16x16x32_bf16 v[124:127], v[80:83], v[180:183], v[124:127]
	v_mfma_f32_16x16x32_bf16 v[108:111], v[56:59], v[192:195], v[108:111]
	v_mfma_f32_16x16x32_bf16 v[104:107], v[80:83], v[192:195], v[104:107]
	v_mfma_f32_16x16x32_bf16 v[88:91], v[56:59], v[200:203], v[88:91]
	v_mfma_f32_16x16x32_bf16 v[84:87], v[80:83], v[200:203], v[84:87]
	v_mfma_f32_16x16x32_bf16 v[148:151], v[60:63], v[176:179], v[148:151]
	v_mfma_f32_16x16x32_bf16 v[144:147], v[100:103], v[176:179], v[144:147]
	v_mfma_f32_16x16x32_bf16 v[128:131], v[60:63], v[184:187], v[128:131]
	v_mfma_f32_16x16x32_bf16 v[124:127], v[100:103], v[184:187], v[124:127]
	v_mfma_f32_16x16x32_bf16 v[108:111], v[60:63], v[196:199], v[108:111]
	v_mfma_f32_16x16x32_bf16 v[104:107], v[100:103], v[196:199], v[104:107]
	v_mfma_f32_16x16x32_bf16 v[88:91], v[60:63], v[204:207], v[88:91]
	v_mfma_f32_16x16x32_bf16 v[84:87], v[100:103], v[204:207], v[84:87]
	s_setprio 0
	s_setprio 1
	v_mfma_f32_16x16x32_bf16 v[136:139], v[120:123], v[172:175], v[136:139]
	v_mfma_f32_16x16x32_bf16 v[132:135], v[152:155], v[172:175], v[132:135]
	v_mfma_f32_16x16x32_bf16 v[116:119], v[120:123], v[180:183], v[116:119]
	v_mfma_f32_16x16x32_bf16 v[112:115], v[152:155], v[180:183], v[112:115]
	v_mfma_f32_16x16x32_bf16 v[96:99], v[120:123], v[192:195], v[96:99]
	v_mfma_f32_16x16x32_bf16 v[92:95], v[152:155], v[192:195], v[92:95]
	v_mfma_f32_16x16x32_bf16 v[76:79], v[120:123], v[200:203], v[76:79]
	v_mfma_f32_16x16x32_bf16 v[72:75], v[152:155], v[200:203], v[72:75]
	v_mfma_f32_16x16x32_bf16 v[136:139], v[140:143], v[176:179], v[136:139]
	v_mfma_f32_16x16x32_bf16 v[132:135], v[156:159], v[176:179], v[132:135]
	v_mfma_f32_16x16x32_bf16 v[116:119], v[140:143], v[184:187], v[116:119]
	v_mfma_f32_16x16x32_bf16 v[112:115], v[156:159], v[184:187], v[112:115]
	v_mfma_f32_16x16x32_bf16 v[96:99], v[140:143], v[196:199], v[96:99]
	v_mfma_f32_16x16x32_bf16 v[92:95], v[156:159], v[196:199], v[92:95]
	v_mfma_f32_16x16x32_bf16 v[76:79], v[140:143], v[204:207], v[76:79]
	v_mfma_f32_16x16x32_bf16 v[72:75], v[156:159], v[204:207], v[72:75]
	s_setprio 0
	s_barrier
	s_add_u32 s30, s24, 0x8000
	s_addc_u32 s31, s25, 0
	s_mov_b32 m0, s87
	v_lshl_add_u64 v[210:211], s[30:31], 0, v[162:163]
	s_add_u32 s24, s24, 0xc000
	ds_read_b128 v[172:175], v191 offset:49152
	ds_read_b128 v[176:179], v191 offset:50176
	ds_read_b128 v[180:183], v191 offset:51200
	ds_read_b128 v[184:187], v191 offset:52224
	ds_read_b128 v[192:195], v191 offset:53248
	ds_read_b128 v[196:199], v191 offset:54272
	ds_read_b128 v[200:203], v191 offset:55296
	ds_read_b128 v[204:207], v191 offset:56320
	global_load_lds_dwordx4 v[210:211], off
	v_lshl_add_u64 v[210:211], s[30:31], 0, v[166:167]
	s_mov_b32 m0, s92
	s_addc_u32 s25, s25, 0
	global_load_lds_dwordx4 v[210:211], off
	v_lshl_add_u64 v[210:211], s[24:25], 0, v[162:163]
	s_mov_b32 m0, s96
	v_lshl_add_u64 v[188:189], v[188:189], 0, s[26:27]
	global_load_lds_dwordx4 v[210:211], off
	v_lshl_add_u64 v[210:211], s[24:25], 0, v[166:167]
	s_mov_b32 m0, s97
	s_nop 0
	global_load_lds_dwordx4 v[210:211], off
	s_mov_b32 m0, s93
	s_nop 0
	global_load_lds_dwordx4 v[188:189], off
	v_lshl_add_u64 v[188:189], v[208:209], 0, s[26:27]
	s_mov_b32 m0, s94
	s_nop 0
	global_load_lds_dwordx4 v[188:189], off
	s_waitcnt vmcnt(8)
	s_waitcnt lgkmcnt(0)
	s_barrier
	s_setprio 1
	s_waitcnt lgkmcnt(0)
	v_mfma_f32_16x16x32_bf16 v[68:71], v[56:59], v[172:175], v[68:71]
	v_mfma_f32_16x16x32_bf16 v[64:67], v[80:83], v[172:175], v[64:67]
	v_mfma_f32_16x16x32_bf16 v[48:51], v[56:59], v[180:183], v[48:51]
	v_mfma_f32_16x16x32_bf16 v[44:47], v[80:83], v[180:183], v[44:47]
	v_mfma_f32_16x16x32_bf16 v[28:31], v[56:59], v[192:195], v[28:31]
	v_mfma_f32_16x16x32_bf16 v[24:27], v[80:83], v[192:195], v[24:27]
	v_mfma_f32_16x16x32_bf16 v[12:15], v[56:59], v[200:203], v[12:15]
	v_mfma_f32_16x16x32_bf16 v[8:11], v[80:83], v[200:203], v[8:11]
	v_mfma_f32_16x16x32_bf16 v[68:71], v[60:63], v[176:179], v[68:71]
	v_mfma_f32_16x16x32_bf16 v[64:67], v[100:103], v[176:179], v[64:67]
	v_mfma_f32_16x16x32_bf16 v[48:51], v[60:63], v[184:187], v[48:51]
	v_mfma_f32_16x16x32_bf16 v[44:47], v[100:103], v[184:187], v[44:47]
	v_mfma_f32_16x16x32_bf16 v[28:31], v[60:63], v[196:199], v[28:31]
	v_mfma_f32_16x16x32_bf16 v[24:27], v[100:103], v[196:199], v[24:27]
	v_mfma_f32_16x16x32_bf16 v[12:15], v[60:63], v[204:207], v[12:15]
	v_mfma_f32_16x16x32_bf16 v[8:11], v[100:103], v[204:207], v[8:11]
	s_setprio 0
	s_setprio 1
	v_mfma_f32_16x16x32_bf16 v[40:43], v[120:123], v[172:175], v[40:43]
	v_mfma_f32_16x16x32_bf16 v[56:59], v[140:143], v[176:179], v[40:43]
	v_mfma_f32_16x16x32_bf16 v[40:43], v[152:155], v[172:175], v[52:55]
	v_mfma_f32_16x16x32_bf16 v[36:39], v[120:123], v[180:183], v[36:39]
	v_mfma_f32_16x16x32_bf16 v[32:35], v[152:155], v[180:183], v[32:35]
	v_mfma_f32_16x16x32_bf16 v[20:23], v[120:123], v[192:195], v[20:23]
	v_mfma_f32_16x16x32_bf16 v[16:19], v[152:155], v[192:195], v[16:19]
	v_mfma_f32_16x16x32_bf16 v[4:7], v[120:123], v[200:203], v[4:7]
	v_mfma_f32_16x16x32_bf16 v[0:3], v[152:155], v[200:203], v[0:3]
	v_mfma_f32_16x16x32_bf16 v[52:55], v[156:159], v[176:179], v[40:43]
	v_mfma_f32_16x16x32_bf16 v[36:39], v[140:143], v[184:187], v[36:39]
	v_mfma_f32_16x16x32_bf16 v[32:35], v[156:159], v[184:187], v[32:35]
	v_mfma_f32_16x16x32_bf16 v[20:23], v[140:143], v[196:199], v[20:23]
	v_mfma_f32_16x16x32_bf16 v[16:19], v[156:159], v[196:199], v[16:19]
	v_mfma_f32_16x16x32_bf16 v[4:7], v[140:143], v[204:207], v[4:7]
	v_mfma_f32_16x16x32_bf16 v[0:3], v[156:159], v[204:207], v[0:3]
	s_setprio 0
	s_barrier
	s_add_i32 s28, s28, 2
	s_add_u32 s17, s17, 0x10000
	s_addc_u32 s19, s19, 0
	s_add_u32 s0, s0, 0x100
	s_addc_u32 s1, s1, 0
	s_cmp_gt_u32 s28, 29
	.p2align	6

.LBB0_1054:
	s_ashr_i32 s41, s40, 31
	s_lshl_b64 s[4:5], s[40:41], 20
	s_add_u32 s44, s16, s4
	s_addc_u32 s45, s17, s5
	s_and_b64 s[4:5], s[36:37], exec
	s_cselect_b32 s4, s45, s51
	s_cselect_b32 s5, s44, s50
	s_ashr_i32 s39, s38, 31
	s_lshl_b64 s[46:47], s[38:39], 20
	s_add_u32 s46, s18, s46
	s_addc_u32 s47, s19, s47
	s_and_b64 s[52:53], s[36:37], exec
	s_cselect_b32 s39, s47, s1
	s_cselect_b32 s41, s46, s0
	s_add_u32 s49, s0, 0x10000
	s_addc_u32 s55, s1, 0
	s_add_u32 s0, s50, 0x80080
	s_addc_u32 s1, s51, 0
	s_mov_b32 s80, -2
	v_add_u32_e32 v140, s28, v215
	v_add_u32_e32 v156, s54, v215
	ds_read_b128 v[128:131], v140
	ds_read_b128 v[132:135], v140 offset:1024
	ds_read_b128 v[136:139], v140 offset:2048
	ds_read_b128 v[140:143], v140 offset:3072
	ds_read_b128 v[144:147], v156
	ds_read_b128 v[148:151], v156 offset:1024
	ds_read_b128 v[152:155], v156 offset:2048
	ds_read_b128 v[156:159], v156 offset:3072
	s_add_u32 s50, s0, 0xfff80080
	s_addc_u32 s51, s1, -1
	s_cmp_eq_u32 s80, 28
	s_cselect_b32 s53, s4, s51
	s_cselect_b32 s52, s5, s50
	s_cselect_b32 s51, s39, s55
	s_cselect_b32 s50, s41, s49
	v_lshl_add_u64 v[204:205], s[0:1], 0, v[180:181]
	s_add_i32 m0, s58, 0xc000
	ds_read_b128 v[160:163], v251
	ds_read_b128 v[164:167], v251 offset:1024
	ds_read_b128 v[168:171], v251 offset:2048
	ds_read_b128 v[184:187], v251 offset:3072
	ds_read_b128 v[188:191], v251 offset:4096
	ds_read_b128 v[192:195], v251 offset:5120
	ds_read_b128 v[196:199], v251 offset:6144
	ds_read_b128 v[200:203], v251 offset:7168
	global_load_lds_dwordx4 v[204:205], off
	v_lshl_add_u64 v[204:205], s[0:1], 0, v[182:183]
	s_add_i32 m0, s58, 0xe000
	s_nop 0
	global_load_lds_dwordx4 v[204:205], off
	s_waitcnt vmcnt(8)
	s_waitcnt lgkmcnt(0)
	s_barrier
	s_setprio 1
	s_waitcnt lgkmcnt(0)
	v_mfma_f32_16x16x32_bf16 v[124:127], v[128:131], v[160:163], 0
	v_mfma_f32_16x16x32_bf16 v[120:123], v[136:139], v[160:163], 0
	v_mfma_f32_16x16x32_bf16 v[116:119], v[128:131], v[168:171], 0
	v_mfma_f32_16x16x32_bf16 v[112:115], v[136:139], v[168:171], 0
	v_mfma_f32_16x16x32_bf16 v[108:111], v[128:131], v[188:191], 0
	v_mfma_f32_16x16x32_bf16 v[104:107], v[136:139], v[188:191], 0
	v_mfma_f32_16x16x32_bf16 v[100:103], v[128:131], v[196:199], 0
	v_mfma_f32_16x16x32_bf16 v[96:99], v[136:139], v[196:199], 0
	v_mfma_f32_16x16x32_bf16 v[124:127], v[132:135], v[164:167], v[124:127]
	v_mfma_f32_16x16x32_bf16 v[120:123], v[140:143], v[164:167], v[120:123]
	v_mfma_f32_16x16x32_bf16 v[116:119], v[132:135], v[184:187], v[116:119]
	v_mfma_f32_16x16x32_bf16 v[112:115], v[140:143], v[184:187], v[112:115]
	v_mfma_f32_16x16x32_bf16 v[108:111], v[132:135], v[192:195], v[108:111]
	v_mfma_f32_16x16x32_bf16 v[104:107], v[140:143], v[192:195], v[104:107]
	v_mfma_f32_16x16x32_bf16 v[100:103], v[132:135], v[200:203], v[100:103]
	v_mfma_f32_16x16x32_bf16 v[96:99], v[140:143], v[200:203], v[96:99]
	s_setprio 0
	s_setprio 1
	v_mfma_f32_16x16x32_bf16 v[60:63], v[144:147], v[160:163], 0
	v_mfma_f32_16x16x32_bf16 v[56:59], v[152:155], v[160:163], 0
	v_mfma_f32_16x16x32_bf16 v[52:55], v[144:147], v[168:171], 0
	v_mfma_f32_16x16x32_bf16 v[48:51], v[152:155], v[168:171], 0
	v_mfma_f32_16x16x32_bf16 v[44:47], v[144:147], v[188:191], 0
	v_mfma_f32_16x16x32_bf16 v[40:43], v[152:155], v[188:191], 0
	v_mfma_f32_16x16x32_bf16 v[36:39], v[144:147], v[196:199], 0
	v_mfma_f32_16x16x32_bf16 v[32:35], v[152:155], v[196:199], 0
	v_mfma_f32_16x16x32_bf16 v[60:63], v[148:151], v[164:167], v[60:63]
	v_mfma_f32_16x16x32_bf16 v[56:59], v[156:159], v[164:167], v[56:59]
	v_mfma_f32_16x16x32_bf16 v[52:55], v[148:151], v[184:187], v[52:55]
	v_mfma_f32_16x16x32_bf16 v[48:51], v[156:159], v[184:187], v[48:51]
	v_mfma_f32_16x16x32_bf16 v[44:47], v[148:151], v[192:195], v[44:47]
	v_mfma_f32_16x16x32_bf16 v[40:43], v[156:159], v[192:195], v[40:43]
	v_mfma_f32_16x16x32_bf16 v[36:39], v[148:151], v[200:203], v[36:39]
	v_mfma_f32_16x16x32_bf16 v[32:35], v[156:159], v[200:203], v[32:35]
	s_setprio 0
	s_barrier
	s_mov_b32 m0, s30
	v_lshl_add_u64 v[204:205], s[50:51], 0, v[174:175]
	s_add_u32 s82, s50, 0x4000
	ds_read_b128 v[160:163], v251 offset:16384
	ds_read_b128 v[164:167], v251 offset:17408
	ds_read_b128 v[168:171], v251 offset:18432
	ds_read_b128 v[184:187], v251 offset:19456
	ds_read_b128 v[188:191], v251 offset:20480
	ds_read_b128 v[192:195], v251 offset:21504
	ds_read_b128 v[196:199], v251 offset:22528
	ds_read_b128 v[200:203], v251 offset:23552
	global_load_lds_dwordx4 v[204:205], off
	v_lshl_add_u64 v[204:205], s[50:51], 0, v[178:179]
	s_mov_b32 m0, s43
	s_addc_u32 s83, s51, 0
	global_load_lds_dwordx4 v[204:205], off
	v_lshl_add_u64 v[204:205], s[82:83], 0, v[174:175]
	s_mov_b32 m0, s56
	v_lshl_add_u64 v[206:207], s[52:53], 0, v[176:177]
	global_load_lds_dwordx4 v[204:205], off
	v_lshl_add_u64 v[204:205], s[82:83], 0, v[178:179]
	s_mov_b32 m0, s57
	s_nop 0
	global_load_lds_dwordx4 v[204:205], off
	v_lshl_add_u64 v[204:205], s[52:53], 0, v[172:173]
	s_mov_b32 m0, s58
	s_nop 0
	global_load_lds_dwordx4 v[204:205], off
	s_mov_b32 m0, s59
	s_nop 0
	global_load_lds_dwordx4 v[206:207], off
	s_waitcnt vmcnt(8)
	s_waitcnt lgkmcnt(0)
	s_barrier
	s_setprio 1
	s_waitcnt lgkmcnt(0)
	v_mfma_f32_16x16x32_bf16 v[92:95], v[128:131], v[160:163], 0
	v_mfma_f32_16x16x32_bf16 v[88:91], v[136:139], v[160:163], 0
	v_mfma_f32_16x16x32_bf16 v[84:87], v[128:131], v[168:171], 0
	v_mfma_f32_16x16x32_bf16 v[80:83], v[136:139], v[168:171], 0
	v_mfma_f32_16x16x32_bf16 v[76:79], v[128:131], v[188:191], 0
	v_mfma_f32_16x16x32_bf16 v[72:75], v[136:139], v[188:191], 0
	v_mfma_f32_16x16x32_bf16 v[68:71], v[128:131], v[196:199], 0
	v_mfma_f32_16x16x32_bf16 v[64:67], v[136:139], v[196:199], 0
	v_mfma_f32_16x16x32_bf16 v[92:95], v[132:135], v[164:167], v[92:95]
	v_mfma_f32_16x16x32_bf16 v[88:91], v[140:143], v[164:167], v[88:91]
	v_mfma_f32_16x16x32_bf16 v[84:87], v[132:135], v[184:187], v[84:87]
	v_mfma_f32_16x16x32_bf16 v[80:83], v[140:143], v[184:187], v[80:83]
	v_mfma_f32_16x16x32_bf16 v[76:79], v[132:135], v[192:195], v[76:79]
	v_mfma_f32_16x16x32_bf16 v[72:75], v[140:143], v[192:195], v[72:75]
	v_mfma_f32_16x16x32_bf16 v[68:71], v[132:135], v[200:203], v[68:71]
	v_mfma_f32_16x16x32_bf16 v[64:67], v[140:143], v[200:203], v[64:67]
	s_setprio 0
	s_setprio 1
	v_mfma_f32_16x16x32_bf16 v[28:31], v[144:147], v[160:163], 0
	v_mfma_f32_16x16x32_bf16 v[24:27], v[152:155], v[160:163], 0
	v_mfma_f32_16x16x32_bf16 v[20:23], v[144:147], v[168:171], 0
	v_mfma_f32_16x16x32_bf16 v[16:19], v[152:155], v[168:171], 0
	v_mfma_f32_16x16x32_bf16 v[12:15], v[144:147], v[188:191], 0
	v_mfma_f32_16x16x32_bf16 v[8:11], v[152:155], v[188:191], 0
	v_mfma_f32_16x16x32_bf16 v[4:7], v[144:147], v[196:199], 0
	v_mfma_f32_16x16x32_bf16 v[0:3], v[152:155], v[196:199], 0
	v_mfma_f32_16x16x32_bf16 v[28:31], v[148:151], v[164:167], v[28:31]
	v_mfma_f32_16x16x32_bf16 v[24:27], v[156:159], v[164:167], v[24:27]
	v_mfma_f32_16x16x32_bf16 v[20:23], v[148:151], v[184:187], v[20:23]
	v_mfma_f32_16x16x32_bf16 v[16:19], v[156:159], v[184:187], v[16:19]
	v_mfma_f32_16x16x32_bf16 v[12:15], v[148:151], v[192:195], v[12:15]
	v_mfma_f32_16x16x32_bf16 v[8:11], v[156:159], v[192:195], v[8:11]
	v_mfma_f32_16x16x32_bf16 v[4:7], v[148:151], v[200:203], v[4:7]
	v_mfma_f32_16x16x32_bf16 v[0:3], v[156:159], v[200:203], v[0:3]
	s_setprio 0
	s_barrier
	v_add_u32_e32 v140, s68, v215
	v_add_u32_e32 v156, s73, v215
	ds_read_b128 v[128:131], v140
	ds_read_b128 v[132:135], v140 offset:1024
	ds_read_b128 v[136:139], v140 offset:2048
	ds_read_b128 v[140:143], v140 offset:3072
	ds_read_b128 v[144:147], v156
	ds_read_b128 v[148:151], v156 offset:1024
	ds_read_b128 v[152:155], v156 offset:2048
	ds_read_b128 v[156:159], v156 offset:3072
	s_add_u32 s52, s52, 0x80000
	s_addc_u32 s53, s53, 0
	s_mov_b32 m0, s60
	v_lshl_add_u64 v[208:209], s[52:53], 0, v[172:173]
	ds_read_b128 v[160:163], v251 offset:32768
	ds_read_b128 v[164:167], v251 offset:33792
	ds_read_b128 v[168:171], v251 offset:34816
	ds_read_b128 v[184:187], v251 offset:35840
	ds_read_b128 v[188:191], v251 offset:36864
	ds_read_b128 v[192:195], v251 offset:37888
	ds_read_b128 v[196:199], v251 offset:38912
	ds_read_b128 v[200:203], v251 offset:39936
	global_load_lds_dwordx4 v[208:209], off
	v_lshl_add_u64 v[208:209], s[52:53], 0, v[176:177]
	s_mov_b32 m0, s61
	s_nop 0
	global_load_lds_dwordx4 v[208:209], off
	s_waitcnt vmcnt(8)
	s_waitcnt lgkmcnt(0)
	s_barrier
	s_setprio 1
	s_waitcnt lgkmcnt(0)
	v_mfma_f32_16x16x32_bf16 v[124:127], v[128:131], v[160:163], v[124:127]
	v_mfma_f32_16x16x32_bf16 v[120:123], v[136:139], v[160:163], v[120:123]
	v_mfma_f32_16x16x32_bf16 v[116:119], v[128:131], v[168:171], v[116:119]
	v_mfma_f32_16x16x32_bf16 v[112:115], v[136:139], v[168:171], v[112:115]
	v_mfma_f32_16x16x32_bf16 v[108:111], v[128:131], v[188:191], v[108:111]
	v_mfma_f32_16x16x32_bf16 v[104:107], v[136:139], v[188:191], v[104:107]
	v_mfma_f32_16x16x32_bf16 v[100:103], v[128:131], v[196:199], v[100:103]
	v_mfma_f32_16x16x32_bf16 v[96:99], v[136:139], v[196:199], v[96:99]
	v_mfma_f32_16x16x32_bf16 v[124:127], v[132:135], v[164:167], v[124:127]
	v_mfma_f32_16x16x32_bf16 v[120:123], v[140:143], v[164:167], v[120:123]
	v_mfma_f32_16x16x32_bf16 v[116:119], v[132:135], v[184:187], v[116:119]
	v_mfma_f32_16x16x32_bf16 v[112:115], v[140:143], v[184:187], v[112:115]
	v_mfma_f32_16x16x32_bf16 v[108:111], v[132:135], v[192:195], v[108:111]
	v_mfma_f32_16x16x32_bf16 v[104:107], v[140:143], v[192:195], v[104:107]
	v_mfma_f32_16x16x32_bf16 v[100:103], v[132:135], v[200:203], v[100:103]
	v_mfma_f32_16x16x32_bf16 v[96:99], v[140:143], v[200:203], v[96:99]
	s_setprio 0
	s_setprio 1
	v_mfma_f32_16x16x32_bf16 v[60:63], v[144:147], v[160:163], v[60:63]
	v_mfma_f32_16x16x32_bf16 v[56:59], v[152:155], v[160:163], v[56:59]
	v_mfma_f32_16x16x32_bf16 v[52:55], v[144:147], v[168:171], v[52:55]
	v_mfma_f32_16x16x32_bf16 v[48:51], v[152:155], v[168:171], v[48:51]
	v_mfma_f32_16x16x32_bf16 v[44:47], v[144:147], v[188:191], v[44:47]
	v_mfma_f32_16x16x32_bf16 v[40:43], v[152:155], v[188:191], v[40:43]
	v_mfma_f32_16x16x32_bf16 v[36:39], v[144:147], v[196:199], v[36:39]
	v_mfma_f32_16x16x32_bf16 v[32:35], v[152:155], v[196:199], v[32:35]
	v_mfma_f32_16x16x32_bf16 v[60:63], v[148:151], v[164:167], v[60:63]
	v_mfma_f32_16x16x32_bf16 v[56:59], v[156:159], v[164:167], v[56:59]
	v_mfma_f32_16x16x32_bf16 v[52:55], v[148:151], v[184:187], v[52:55]
	v_mfma_f32_16x16x32_bf16 v[48:51], v[156:159], v[184:187], v[48:51]
	v_mfma_f32_16x16x32_bf16 v[44:47], v[148:151], v[192:195], v[44:47]
	v_mfma_f32_16x16x32_bf16 v[40:43], v[156:159], v[192:195], v[40:43]
	v_mfma_f32_16x16x32_bf16 v[36:39], v[148:151], v[200:203], v[36:39]
	v_mfma_f32_16x16x32_bf16 v[32:35], v[156:159], v[200:203], v[32:35]
	s_setprio 0
	s_barrier
	s_add_u32 s52, s50, 0x8000
	s_addc_u32 s53, s51, 0
	s_mov_b32 m0, s69
	v_lshl_add_u64 v[208:209], s[52:53], 0, v[174:175]
	s_add_u32 s50, s50, 0xc000
	ds_read_b128 v[160:163], v251 offset:49152
	ds_read_b128 v[164:167], v251 offset:50176
	ds_read_b128 v[168:171], v251 offset:51200
	ds_read_b128 v[184:187], v251 offset:52224
	ds_read_b128 v[188:191], v251 offset:53248
	ds_read_b128 v[192:195], v251 offset:54272
	ds_read_b128 v[196:199], v251 offset:55296
	ds_read_b128 v[200:203], v251 offset:56320
	global_load_lds_dwordx4 v[208:209], off
	v_lshl_add_u64 v[208:209], s[52:53], 0, v[178:179]
	s_mov_b32 m0, s70
	s_addc_u32 s51, s51, 0
	global_load_lds_dwordx4 v[208:209], off
	v_lshl_add_u64 v[208:209], s[50:51], 0, v[174:175]
	s_mov_b32 m0, s74
	v_lshl_add_u64 v[204:205], v[204:205], 0, s[26:27]
	global_load_lds_dwordx4 v[208:209], off
	v_lshl_add_u64 v[208:209], s[50:51], 0, v[178:179]
	s_mov_b32 m0, s75
	s_nop 0
	global_load_lds_dwordx4 v[208:209], off
	s_mov_b32 m0, s71
	s_nop 0
	global_load_lds_dwordx4 v[204:205], off
	v_lshl_add_u64 v[204:205], v[206:207], 0, s[26:27]
	s_mov_b32 m0, s72
	s_nop 0
	global_load_lds_dwordx4 v[204:205], off
	s_waitcnt vmcnt(8)
	s_waitcnt lgkmcnt(0)
	s_barrier
	s_setprio 1
	s_waitcnt lgkmcnt(0)
	v_mfma_f32_16x16x32_bf16 v[92:95], v[128:131], v[160:163], v[92:95]
	v_mfma_f32_16x16x32_bf16 v[88:91], v[136:139], v[160:163], v[88:91]
	v_mfma_f32_16x16x32_bf16 v[84:87], v[128:131], v[168:171], v[84:87]
	v_mfma_f32_16x16x32_bf16 v[80:83], v[136:139], v[168:171], v[80:83]
	v_mfma_f32_16x16x32_bf16 v[76:79], v[128:131], v[188:191], v[76:79]
	v_mfma_f32_16x16x32_bf16 v[72:75], v[136:139], v[188:191], v[72:75]
	v_mfma_f32_16x16x32_bf16 v[68:71], v[128:131], v[196:199], v[68:71]
	v_mfma_f32_16x16x32_bf16 v[64:67], v[136:139], v[196:199], v[64:67]
	v_mfma_f32_16x16x32_bf16 v[92:95], v[132:135], v[164:167], v[92:95]
	v_mfma_f32_16x16x32_bf16 v[88:91], v[140:143], v[164:167], v[88:91]
	v_mfma_f32_16x16x32_bf16 v[84:87], v[132:135], v[184:187], v[84:87]
	v_mfma_f32_16x16x32_bf16 v[80:83], v[140:143], v[184:187], v[80:83]
	v_mfma_f32_16x16x32_bf16 v[76:79], v[132:135], v[192:195], v[76:79]
	v_mfma_f32_16x16x32_bf16 v[72:75], v[140:143], v[192:195], v[72:75]
	v_mfma_f32_16x16x32_bf16 v[68:71], v[132:135], v[200:203], v[68:71]
	v_mfma_f32_16x16x32_bf16 v[64:67], v[140:143], v[200:203], v[64:67]
	s_setprio 0
	s_setprio 1
	v_mfma_f32_16x16x32_bf16 v[28:31], v[144:147], v[160:163], v[28:31]
	v_mfma_f32_16x16x32_bf16 v[24:27], v[152:155], v[160:163], v[24:27]
	v_mfma_f32_16x16x32_bf16 v[20:23], v[144:147], v[168:171], v[20:23]
	v_mfma_f32_16x16x32_bf16 v[16:19], v[152:155], v[168:171], v[16:19]
	v_mfma_f32_16x16x32_bf16 v[12:15], v[144:147], v[188:191], v[12:15]
	v_mfma_f32_16x16x32_bf16 v[8:11], v[152:155], v[188:191], v[8:11]
	v_mfma_f32_16x16x32_bf16 v[4:7], v[144:147], v[196:199], v[4:7]
	v_mfma_f32_16x16x32_bf16 v[0:3], v[152:155], v[196:199], v[0:3]
	v_mfma_f32_16x16x32_bf16 v[28:31], v[148:151], v[164:167], v[28:31]
	v_mfma_f32_16x16x32_bf16 v[24:27], v[156:159], v[164:167], v[24:27]
	v_mfma_f32_16x16x32_bf16 v[20:23], v[148:151], v[184:187], v[20:23]
	v_mfma_f32_16x16x32_bf16 v[16:19], v[156:159], v[184:187], v[16:19]
	v_mfma_f32_16x16x32_bf16 v[12:15], v[148:151], v[192:195], v[12:15]
	v_mfma_f32_16x16x32_bf16 v[8:11], v[156:159], v[192:195], v[8:11]
	v_mfma_f32_16x16x32_bf16 v[4:7], v[148:151], v[200:203], v[4:7]
	v_mfma_f32_16x16x32_bf16 v[0:3], v[156:159], v[200:203], v[0:3]
	s_setprio 0
	s_barrier
	s_add_i32 s80, s80, 2
	s_add_u32 s49, s49, 0x10000
	s_addc_u32 s55, s55, 0
	s_add_u32 s0, s0, 0x100
	s_addc_u32 s1, s1, 0
	s_cmp_gt_u32 s80, 29
	.p2align	6

.LBB0_1172:
	s_ashr_i32 s39, s38, 31
	s_lshl_b64 s[4:5], s[38:39], 20
	s_add_u32 s40, s18, s4
	s_addc_u32 s41, s19, s5
	s_and_b64 s[4:5], s[36:37], exec
	s_cselect_b32 s4, s41, s1
	s_cselect_b32 s5, s40, s0
	s_ashr_i32 s35, s34, 31
	s_lshl_b64 s[42:43], s[34:35], 20
	s_add_u32 s42, s16, s42
	s_addc_u32 s43, s17, s43
	s_and_b64 s[48:49], s[36:37], exec
	s_cselect_b32 s35, s43, s47
	s_cselect_b32 s39, s42, s46
	s_add_u32 s76, s46, 0x10000
	s_addc_u32 s77, s47, 0
	s_mov_b32 s78, -2
	v_add_u32_e32 v124, s28, v156
	v_add_u32_e32 v170, s45, v156
	ds_read_b128 v[108:111], v124
	ds_read_b128 v[112:115], v124 offset:1024
	ds_read_b128 v[120:123], v124 offset:2048
	ds_read_b128 v[124:127], v124 offset:3072
	ds_read_b128 v[158:161], v170
	ds_read_b128 v[162:165], v170 offset:1024
	ds_read_b128 v[166:169], v170 offset:2048
	ds_read_b128 v[170:173], v170 offset:3072
	s_add_u32 s46, s0, 0x10000
	s_addc_u32 s47, s1, 0
	s_cmp_eq_u32 s78, 28
	s_cselect_b32 s52, s5, s46
	s_cselect_b32 s53, s4, s47
	s_cselect_b32 s50, s39, s76
	s_cselect_b32 s51, s35, s77
	s_add_u32 s48, s52, 0x8000
	s_addc_u32 s49, s53, 0
	v_lshl_add_u64 v[206:207], s[0:1], 0, v[152:153]
	s_add_i32 m0, s56, 0xc000
	ds_read_b128 v[174:177], v157
	ds_read_b128 v[178:181], v157 offset:1024
	ds_read_b128 v[182:185], v157 offset:2048
	ds_read_b128 v[186:189], v157 offset:3072
	ds_read_b128 v[190:193], v157 offset:4096
	ds_read_b128 v[194:197], v157 offset:5120
	ds_read_b128 v[198:201], v157 offset:6144
	ds_read_b128 v[202:205], v157 offset:7168
	global_load_lds_dwordx4 v[206:207], off
	v_lshl_add_u64 v[206:207], s[0:1], 0, v[154:155]
	s_add_i32 m0, s56, 0xe000
	s_nop 0
	global_load_lds_dwordx4 v[206:207], off
	s_waitcnt vmcnt(8)
	s_waitcnt lgkmcnt(0)
	s_barrier
	s_setprio 1
	s_waitcnt lgkmcnt(0)
	v_mfma_f32_16x16x32_bf16 v[140:143], v[108:111], v[174:177], 0
	v_mfma_f32_16x16x32_bf16 v[136:139], v[120:123], v[174:177], 0
	v_mfma_f32_16x16x32_bf16 v[116:119], v[108:111], v[182:185], 0
	v_mfma_f32_16x16x32_bf16 v[104:107], v[120:123], v[182:185], 0
	v_mfma_f32_16x16x32_bf16 v[92:95], v[108:111], v[190:193], 0
	v_mfma_f32_16x16x32_bf16 v[88:91], v[120:123], v[190:193], 0
	v_mfma_f32_16x16x32_bf16 v[76:79], v[108:111], v[198:201], 0
	v_mfma_f32_16x16x32_bf16 v[72:75], v[120:123], v[198:201], 0
	v_mfma_f32_16x16x32_bf16 v[140:143], v[112:115], v[178:181], v[140:143]
	v_mfma_f32_16x16x32_bf16 v[136:139], v[124:127], v[178:181], v[136:139]
	v_mfma_f32_16x16x32_bf16 v[116:119], v[112:115], v[186:189], v[116:119]
	v_mfma_f32_16x16x32_bf16 v[104:107], v[124:127], v[186:189], v[104:107]
	v_mfma_f32_16x16x32_bf16 v[92:95], v[112:115], v[194:197], v[92:95]
	v_mfma_f32_16x16x32_bf16 v[88:91], v[124:127], v[194:197], v[88:91]
	v_mfma_f32_16x16x32_bf16 v[76:79], v[112:115], v[202:205], v[76:79]
	v_mfma_f32_16x16x32_bf16 v[72:75], v[124:127], v[202:205], v[72:75]
	s_setprio 0
	s_setprio 1
	v_mfma_f32_16x16x32_bf16 v[132:135], v[158:161], v[174:177], 0
	v_mfma_f32_16x16x32_bf16 v[128:131], v[166:169], v[174:177], 0
	v_mfma_f32_16x16x32_bf16 v[100:103], v[158:161], v[182:185], 0
	v_mfma_f32_16x16x32_bf16 v[96:99], v[166:169], v[182:185], 0
	v_mfma_f32_16x16x32_bf16 v[84:87], v[158:161], v[190:193], 0
	v_mfma_f32_16x16x32_bf16 v[80:83], v[166:169], v[190:193], 0
	v_mfma_f32_16x16x32_bf16 v[68:71], v[158:161], v[198:201], 0
	v_mfma_f32_16x16x32_bf16 v[64:67], v[166:169], v[198:201], 0
	v_mfma_f32_16x16x32_bf16 v[132:135], v[162:165], v[178:181], v[132:135]
	v_mfma_f32_16x16x32_bf16 v[128:131], v[170:173], v[178:181], v[128:131]
	v_mfma_f32_16x16x32_bf16 v[100:103], v[162:165], v[186:189], v[100:103]
	v_mfma_f32_16x16x32_bf16 v[96:99], v[170:173], v[186:189], v[96:99]
	v_mfma_f32_16x16x32_bf16 v[84:87], v[162:165], v[194:197], v[84:87]
	v_mfma_f32_16x16x32_bf16 v[80:83], v[170:173], v[194:197], v[80:83]
	v_mfma_f32_16x16x32_bf16 v[68:71], v[162:165], v[202:205], v[68:71]
	v_mfma_f32_16x16x32_bf16 v[64:67], v[170:173], v[202:205], v[64:67]
	s_setprio 0
	s_barrier
	s_mov_b32 m0, s30
	v_lshl_add_u64 v[206:207], s[50:51], 0, v[146:147]
	s_add_u32 s0, s50, 0x4000
	ds_read_b128 v[174:177], v157 offset:16384
	ds_read_b128 v[178:181], v157 offset:17408
	ds_read_b128 v[182:185], v157 offset:18432
	ds_read_b128 v[186:189], v157 offset:19456
	ds_read_b128 v[190:193], v157 offset:20480
	ds_read_b128 v[194:197], v157 offset:21504
	ds_read_b128 v[198:201], v157 offset:22528
	ds_read_b128 v[202:205], v157 offset:23552
	global_load_lds_dwordx4 v[206:207], off
	v_lshl_add_u64 v[206:207], s[50:51], 0, v[150:151]
	s_mov_b32 m0, s31
	s_addc_u32 s1, s51, 0
	global_load_lds_dwordx4 v[206:207], off
	v_lshl_add_u64 v[206:207], s[0:1], 0, v[146:147]
	s_mov_b32 m0, s54
	s_nop 0
	global_load_lds_dwordx4 v[206:207], off
	v_lshl_add_u64 v[206:207], s[0:1], 0, v[150:151]
	s_mov_b32 m0, s55
	s_nop 0
	global_load_lds_dwordx4 v[206:207], off
	v_lshl_add_u64 v[206:207], s[52:53], 0, v[144:145]
	s_mov_b32 m0, s56
	s_nop 0
	global_load_lds_dwordx4 v[206:207], off
	v_lshl_add_u64 v[206:207], s[52:53], 0, v[148:149]
	s_mov_b32 m0, s57
	s_nop 0
	global_load_lds_dwordx4 v[206:207], off
	s_waitcnt vmcnt(8)
	s_waitcnt lgkmcnt(0)
	s_barrier
	s_setprio 1
	s_waitcnt lgkmcnt(0)
	v_mfma_f32_16x16x32_bf16 v[60:63], v[108:111], v[174:177], 0
	v_mfma_f32_16x16x32_bf16 v[56:59], v[120:123], v[174:177], 0
	v_mfma_f32_16x16x32_bf16 v[44:47], v[108:111], v[182:185], 0
	v_mfma_f32_16x16x32_bf16 v[40:43], v[120:123], v[182:185], 0
	v_mfma_f32_16x16x32_bf16 v[28:31], v[108:111], v[190:193], 0
	v_mfma_f32_16x16x32_bf16 v[24:27], v[120:123], v[190:193], 0
	v_mfma_f32_16x16x32_bf16 v[12:15], v[108:111], v[198:201], 0
	v_mfma_f32_16x16x32_bf16 v[8:11], v[120:123], v[198:201], 0
	v_mfma_f32_16x16x32_bf16 v[60:63], v[112:115], v[178:181], v[60:63]
	v_mfma_f32_16x16x32_bf16 v[56:59], v[124:127], v[178:181], v[56:59]
	v_mfma_f32_16x16x32_bf16 v[44:47], v[112:115], v[186:189], v[44:47]
	v_mfma_f32_16x16x32_bf16 v[40:43], v[124:127], v[186:189], v[40:43]
	v_mfma_f32_16x16x32_bf16 v[28:31], v[112:115], v[194:197], v[28:31]
	v_mfma_f32_16x16x32_bf16 v[24:27], v[124:127], v[194:197], v[24:27]
	v_mfma_f32_16x16x32_bf16 v[12:15], v[112:115], v[202:205], v[12:15]
	v_mfma_f32_16x16x32_bf16 v[8:11], v[124:127], v[202:205], v[8:11]
	s_setprio 0
	s_setprio 1
	v_mfma_f32_16x16x32_bf16 v[52:55], v[158:161], v[174:177], 0
	v_mfma_f32_16x16x32_bf16 v[48:51], v[166:169], v[174:177], 0
	v_mfma_f32_16x16x32_bf16 v[36:39], v[158:161], v[182:185], 0
	v_mfma_f32_16x16x32_bf16 v[32:35], v[166:169], v[182:185], 0
	v_mfma_f32_16x16x32_bf16 v[20:23], v[158:161], v[190:193], 0
	v_mfma_f32_16x16x32_bf16 v[16:19], v[166:169], v[190:193], 0
	v_mfma_f32_16x16x32_bf16 v[4:7], v[158:161], v[198:201], 0
	v_mfma_f32_16x16x32_bf16 v[0:3], v[166:169], v[198:201], 0
	v_mfma_f32_16x16x32_bf16 v[52:55], v[162:165], v[178:181], v[52:55]
	v_mfma_f32_16x16x32_bf16 v[48:51], v[170:173], v[178:181], v[48:51]
	v_mfma_f32_16x16x32_bf16 v[36:39], v[162:165], v[186:189], v[36:39]
	v_mfma_f32_16x16x32_bf16 v[32:35], v[170:173], v[186:189], v[32:35]
	v_mfma_f32_16x16x32_bf16 v[20:23], v[162:165], v[194:197], v[20:23]
	v_mfma_f32_16x16x32_bf16 v[16:19], v[170:173], v[194:197], v[16:19]
	v_mfma_f32_16x16x32_bf16 v[4:7], v[162:165], v[202:205], v[4:7]
	v_mfma_f32_16x16x32_bf16 v[0:3], v[170:173], v[202:205], v[0:3]
	s_setprio 0
	s_barrier
	v_add_u32_e32 v124, s62, v156
	v_add_u32_e32 v170, s67, v156
	ds_read_b128 v[108:111], v124
	ds_read_b128 v[112:115], v124 offset:1024
	ds_read_b128 v[120:123], v124 offset:2048
	ds_read_b128 v[124:127], v124 offset:3072
	ds_read_b128 v[158:161], v170
	ds_read_b128 v[162:165], v170 offset:1024
	ds_read_b128 v[166:169], v170 offset:2048
	ds_read_b128 v[170:173], v170 offset:3072
	s_add_u32 s0, s52, 0x4000
	s_addc_u32 s1, s53, 0
	s_mov_b32 m0, s58
	v_lshl_add_u64 v[206:207], s[0:1], 0, v[144:145]
	ds_read_b128 v[174:177], v157 offset:32768
	ds_read_b128 v[178:181], v157 offset:33792
	ds_read_b128 v[182:185], v157 offset:34816
	ds_read_b128 v[186:189], v157 offset:35840
	ds_read_b128 v[190:193], v157 offset:36864
	ds_read_b128 v[194:197], v157 offset:37888
	ds_read_b128 v[198:201], v157 offset:38912
	ds_read_b128 v[202:205], v157 offset:39936
	global_load_lds_dwordx4 v[206:207], off
	v_lshl_add_u64 v[206:207], s[0:1], 0, v[148:149]
	s_mov_b32 m0, s59
	s_nop 0
	global_load_lds_dwordx4 v[206:207], off
	s_waitcnt vmcnt(8)
	s_waitcnt lgkmcnt(0)
	s_barrier
	s_setprio 1
	s_waitcnt lgkmcnt(0)
	v_mfma_f32_16x16x32_bf16 v[140:143], v[108:111], v[174:177], v[140:143]
	v_mfma_f32_16x16x32_bf16 v[136:139], v[120:123], v[174:177], v[136:139]
	v_mfma_f32_16x16x32_bf16 v[116:119], v[108:111], v[182:185], v[116:119]
	v_mfma_f32_16x16x32_bf16 v[104:107], v[120:123], v[182:185], v[104:107]
	v_mfma_f32_16x16x32_bf16 v[92:95], v[108:111], v[190:193], v[92:95]
	v_mfma_f32_16x16x32_bf16 v[88:91], v[120:123], v[190:193], v[88:91]
	v_mfma_f32_16x16x32_bf16 v[76:79], v[108:111], v[198:201], v[76:79]
	v_mfma_f32_16x16x32_bf16 v[72:75], v[120:123], v[198:201], v[72:75]
	v_mfma_f32_16x16x32_bf16 v[140:143], v[112:115], v[178:181], v[140:143]
	v_mfma_f32_16x16x32_bf16 v[136:139], v[124:127], v[178:181], v[136:139]
	v_mfma_f32_16x16x32_bf16 v[116:119], v[112:115], v[186:189], v[116:119]
	v_mfma_f32_16x16x32_bf16 v[104:107], v[124:127], v[186:189], v[104:107]
	v_mfma_f32_16x16x32_bf16 v[92:95], v[112:115], v[194:197], v[92:95]
	v_mfma_f32_16x16x32_bf16 v[88:91], v[124:127], v[194:197], v[88:91]
	v_mfma_f32_16x16x32_bf16 v[76:79], v[112:115], v[202:205], v[76:79]
	v_mfma_f32_16x16x32_bf16 v[72:75], v[124:127], v[202:205], v[72:75]
	s_setprio 0
	s_setprio 1
	v_mfma_f32_16x16x32_bf16 v[132:135], v[158:161], v[174:177], v[132:135]
	v_mfma_f32_16x16x32_bf16 v[128:131], v[166:169], v[174:177], v[128:131]
	v_mfma_f32_16x16x32_bf16 v[100:103], v[158:161], v[182:185], v[100:103]
	v_mfma_f32_16x16x32_bf16 v[96:99], v[166:169], v[182:185], v[96:99]
	v_mfma_f32_16x16x32_bf16 v[84:87], v[158:161], v[190:193], v[84:87]
	v_mfma_f32_16x16x32_bf16 v[80:83], v[166:169], v[190:193], v[80:83]
	v_mfma_f32_16x16x32_bf16 v[68:71], v[158:161], v[198:201], v[68:71]
	v_mfma_f32_16x16x32_bf16 v[64:67], v[166:169], v[198:201], v[64:67]
	v_mfma_f32_16x16x32_bf16 v[132:135], v[162:165], v[178:181], v[132:135]
	v_mfma_f32_16x16x32_bf16 v[128:131], v[170:173], v[178:181], v[128:131]
	v_mfma_f32_16x16x32_bf16 v[100:103], v[162:165], v[186:189], v[100:103]
	v_mfma_f32_16x16x32_bf16 v[96:99], v[170:173], v[186:189], v[96:99]
	v_mfma_f32_16x16x32_bf16 v[84:87], v[162:165], v[194:197], v[84:87]
	v_mfma_f32_16x16x32_bf16 v[80:83], v[170:173], v[194:197], v[80:83]
	v_mfma_f32_16x16x32_bf16 v[68:71], v[162:165], v[202:205], v[68:71]
	v_mfma_f32_16x16x32_bf16 v[64:67], v[170:173], v[202:205], v[64:67]
	s_setprio 0
	s_barrier
	s_add_u32 s0, s50, 0x8000
	s_addc_u32 s1, s51, 0
	s_mov_b32 m0, s63
	v_lshl_add_u64 v[206:207], s[0:1], 0, v[146:147]
	ds_read_b128 v[174:177], v157 offset:49152
	ds_read_b128 v[178:181], v157 offset:50176
	ds_read_b128 v[182:185], v157 offset:51200
	ds_read_b128 v[186:189], v157 offset:52224
	ds_read_b128 v[190:193], v157 offset:53248
	ds_read_b128 v[194:197], v157 offset:54272
	ds_read_b128 v[198:201], v157 offset:55296
	ds_read_b128 v[202:205], v157 offset:56320
	global_load_lds_dwordx4 v[206:207], off
	v_lshl_add_u64 v[206:207], s[0:1], 0, v[150:151]
	s_add_u32 s0, s50, 0xc000
	s_mov_b32 m0, s64
	s_addc_u32 s1, s51, 0
	global_load_lds_dwordx4 v[206:207], off
	v_lshl_add_u64 v[206:207], s[0:1], 0, v[146:147]
	s_mov_b32 m0, s68
	s_nop 0
	global_load_lds_dwordx4 v[206:207], off
	v_lshl_add_u64 v[206:207], s[0:1], 0, v[150:151]
	s_mov_b32 m0, s69
	s_nop 0
	global_load_lds_dwordx4 v[206:207], off
	v_lshl_add_u64 v[206:207], s[48:49], 0, v[144:145]
	s_mov_b32 m0, s65
	s_nop 0
	global_load_lds_dwordx4 v[206:207], off
	v_lshl_add_u64 v[206:207], s[48:49], 0, v[148:149]
	s_mov_b32 m0, s66
	s_nop 0
	global_load_lds_dwordx4 v[206:207], off
	s_waitcnt vmcnt(8)
	s_waitcnt lgkmcnt(0)
	s_barrier
	s_setprio 1
	s_waitcnt lgkmcnt(0)
	v_mfma_f32_16x16x32_bf16 v[60:63], v[108:111], v[174:177], v[60:63]
	v_mfma_f32_16x16x32_bf16 v[56:59], v[120:123], v[174:177], v[56:59]
	v_mfma_f32_16x16x32_bf16 v[44:47], v[108:111], v[182:185], v[44:47]
	v_mfma_f32_16x16x32_bf16 v[40:43], v[120:123], v[182:185], v[40:43]
	v_mfma_f32_16x16x32_bf16 v[28:31], v[108:111], v[190:193], v[28:31]
	v_mfma_f32_16x16x32_bf16 v[24:27], v[120:123], v[190:193], v[24:27]
	v_mfma_f32_16x16x32_bf16 v[12:15], v[108:111], v[198:201], v[12:15]
	v_mfma_f32_16x16x32_bf16 v[8:11], v[120:123], v[198:201], v[8:11]
	v_mfma_f32_16x16x32_bf16 v[60:63], v[112:115], v[178:181], v[60:63]
	v_mfma_f32_16x16x32_bf16 v[56:59], v[124:127], v[178:181], v[56:59]
	v_mfma_f32_16x16x32_bf16 v[44:47], v[112:115], v[186:189], v[44:47]
	v_mfma_f32_16x16x32_bf16 v[40:43], v[124:127], v[186:189], v[40:43]
	v_mfma_f32_16x16x32_bf16 v[28:31], v[112:115], v[194:197], v[28:31]
	v_mfma_f32_16x16x32_bf16 v[24:27], v[124:127], v[194:197], v[24:27]
	v_mfma_f32_16x16x32_bf16 v[12:15], v[112:115], v[202:205], v[12:15]
	v_mfma_f32_16x16x32_bf16 v[8:11], v[124:127], v[202:205], v[8:11]
	s_setprio 0
	s_setprio 1
	v_mfma_f32_16x16x32_bf16 v[52:55], v[158:161], v[174:177], v[52:55]
	v_mfma_f32_16x16x32_bf16 v[48:51], v[166:169], v[174:177], v[48:51]
	v_mfma_f32_16x16x32_bf16 v[36:39], v[158:161], v[182:185], v[36:39]
	v_mfma_f32_16x16x32_bf16 v[32:35], v[166:169], v[182:185], v[32:35]
	v_mfma_f32_16x16x32_bf16 v[20:23], v[158:161], v[190:193], v[20:23]
	v_mfma_f32_16x16x32_bf16 v[16:19], v[166:169], v[190:193], v[16:19]
	v_mfma_f32_16x16x32_bf16 v[4:7], v[158:161], v[198:201], v[4:7]
	v_mfma_f32_16x16x32_bf16 v[0:3], v[166:169], v[198:201], v[0:3]
	v_mfma_f32_16x16x32_bf16 v[52:55], v[162:165], v[178:181], v[52:55]
	v_mfma_f32_16x16x32_bf16 v[48:51], v[170:173], v[178:181], v[48:51]
	v_mfma_f32_16x16x32_bf16 v[36:39], v[162:165], v[186:189], v[36:39]
	v_mfma_f32_16x16x32_bf16 v[32:35], v[170:173], v[186:189], v[32:35]
	v_mfma_f32_16x16x32_bf16 v[20:23], v[162:165], v[194:197], v[20:23]
	v_mfma_f32_16x16x32_bf16 v[16:19], v[170:173], v[194:197], v[16:19]
	v_mfma_f32_16x16x32_bf16 v[4:7], v[162:165], v[202:205], v[4:7]
	v_mfma_f32_16x16x32_bf16 v[0:3], v[170:173], v[202:205], v[0:3]
	s_setprio 0
	s_barrier
	s_add_i32 s78, s78, 2
	s_add_u32 s76, s76, 0x10000
	s_addc_u32 s77, s77, 0
	s_cmp_gt_u32 s78, 29
	s_mov_b64 s[0:1], s[46:47]
	.p2align	6

.LBB0_1247:
	s_ashr_i32 s35, s34, 31
	s_lshl_b64 s[4:5], s[34:35], 22
	s_add_u32 s38, s17, s4
	s_addc_u32 s39, s18, s5
	s_and_b64 s[4:5], s[36:37], exec
	s_cselect_b32 s4, s39, s1
	s_cselect_b32 s5, s38, s0
	s_ashr_i32 s25, s24, 31
	s_lshl_b64 s[40:41], s[24:25], 22
	s_add_u32 s40, s19, s40
	s_addc_u32 s41, s28, s41
	s_and_b64 s[46:47], s[36:37], exec
	s_cselect_b32 s25, s41, s45
	s_cselect_b32 s35, s40, s44
	s_add_u32 s74, s44, 0x10000
	s_addc_u32 s75, s45, 0
	s_mov_b32 s76, -2
	v_add_u32_e32 v92, s30, v206
	v_add_u32_e32 v156, s52, v206
	ds_read_b128 v[72:75], v92
	ds_read_b128 v[76:79], v92 offset:1024
	ds_read_b128 v[84:87], v92 offset:2048
	ds_read_b128 v[92:95], v92 offset:3072
	ds_read_b128 v[144:147], v156
	ds_read_b128 v[148:151], v156 offset:1024
	ds_read_b128 v[152:155], v156 offset:2048
	ds_read_b128 v[156:159], v156 offset:3072
	s_add_u32 s44, s0, 0x10000
	s_addc_u32 s45, s1, 0
	s_cmpk_eq_i32 s76, 0x7c
	s_cselect_b32 s50, s5, s44
	s_cselect_b32 s51, s4, s45
	s_cselect_b32 s48, s35, s74
	s_cselect_b32 s49, s25, s75
	s_add_u32 s46, s50, 0x8000
	s_addc_u32 s47, s51, 0
	v_lshl_add_u64 v[204:205], s[0:1], 0, v[180:181]
	s_add_i32 m0, s56, 0xc000
	ds_read_b128 v[160:163], v207
	ds_read_b128 v[164:167], v207 offset:1024
	ds_read_b128 v[168:171], v207 offset:2048
	ds_read_b128 v[184:187], v207 offset:3072
	ds_read_b128 v[188:191], v207 offset:4096
	ds_read_b128 v[192:195], v207 offset:5120
	ds_read_b128 v[196:199], v207 offset:6144
	ds_read_b128 v[200:203], v207 offset:7168
	global_load_lds_dwordx4 v[204:205], off
	v_lshl_add_u64 v[204:205], s[0:1], 0, v[182:183]
	s_add_i32 m0, s56, 0xe000
	s_nop 0
	global_load_lds_dwordx4 v[204:205], off
	s_waitcnt vmcnt(8)
	s_waitcnt lgkmcnt(0)
	s_barrier
	s_setprio 1
	s_waitcnt lgkmcnt(0)
	v_mfma_f32_16x16x32_bf16 v[140:143], v[72:75], v[160:163], 0
	v_mfma_f32_16x16x32_bf16 v[136:139], v[84:87], v[160:163], 0
	v_mfma_f32_16x16x32_bf16 v[124:127], v[72:75], v[168:171], 0
	v_mfma_f32_16x16x32_bf16 v[120:123], v[84:87], v[168:171], 0
	v_mfma_f32_16x16x32_bf16 v[108:111], v[72:75], v[188:191], 0
	v_mfma_f32_16x16x32_bf16 v[104:107], v[84:87], v[188:191], 0
	v_mfma_f32_16x16x32_bf16 v[88:91], v[72:75], v[196:199], 0
	v_mfma_f32_16x16x32_bf16 v[80:83], v[84:87], v[196:199], 0
	v_mfma_f32_16x16x32_bf16 v[140:143], v[76:79], v[164:167], v[140:143]
	v_mfma_f32_16x16x32_bf16 v[136:139], v[92:95], v[164:167], v[136:139]
	v_mfma_f32_16x16x32_bf16 v[124:127], v[76:79], v[184:187], v[124:127]
	v_mfma_f32_16x16x32_bf16 v[120:123], v[92:95], v[184:187], v[120:123]
	v_mfma_f32_16x16x32_bf16 v[108:111], v[76:79], v[192:195], v[108:111]
	v_mfma_f32_16x16x32_bf16 v[104:107], v[92:95], v[192:195], v[104:107]
	v_mfma_f32_16x16x32_bf16 v[88:91], v[76:79], v[200:203], v[88:91]
	v_mfma_f32_16x16x32_bf16 v[80:83], v[92:95], v[200:203], v[80:83]
	s_setprio 0
	s_setprio 1
	v_mfma_f32_16x16x32_bf16 v[132:135], v[144:147], v[160:163], 0
	v_mfma_f32_16x16x32_bf16 v[128:131], v[152:155], v[160:163], 0
	v_mfma_f32_16x16x32_bf16 v[116:119], v[144:147], v[168:171], 0
	v_mfma_f32_16x16x32_bf16 v[112:115], v[152:155], v[168:171], 0
	v_mfma_f32_16x16x32_bf16 v[100:103], v[144:147], v[188:191], 0
	v_mfma_f32_16x16x32_bf16 v[96:99], v[152:155], v[188:191], 0
	v_mfma_f32_16x16x32_bf16 v[68:71], v[144:147], v[196:199], 0
	v_mfma_f32_16x16x32_bf16 v[64:67], v[152:155], v[196:199], 0
	v_mfma_f32_16x16x32_bf16 v[132:135], v[148:151], v[164:167], v[132:135]
	v_mfma_f32_16x16x32_bf16 v[128:131], v[156:159], v[164:167], v[128:131]
	v_mfma_f32_16x16x32_bf16 v[116:119], v[148:151], v[184:187], v[116:119]
	v_mfma_f32_16x16x32_bf16 v[112:115], v[156:159], v[184:187], v[112:115]
	v_mfma_f32_16x16x32_bf16 v[100:103], v[148:151], v[192:195], v[100:103]
	v_mfma_f32_16x16x32_bf16 v[96:99], v[156:159], v[192:195], v[96:99]
	v_mfma_f32_16x16x32_bf16 v[68:71], v[148:151], v[200:203], v[68:71]
	v_mfma_f32_16x16x32_bf16 v[64:67], v[156:159], v[200:203], v[64:67]
	s_setprio 0
	s_barrier
	s_mov_b32 m0, s31
	v_lshl_add_u64 v[204:205], s[48:49], 0, v[174:175]
	s_add_u32 s0, s48, 0x4000
	ds_read_b128 v[160:163], v207 offset:16384
	ds_read_b128 v[164:167], v207 offset:17408
	ds_read_b128 v[168:171], v207 offset:18432
	ds_read_b128 v[184:187], v207 offset:19456
	ds_read_b128 v[188:191], v207 offset:20480
	ds_read_b128 v[192:195], v207 offset:21504
	ds_read_b128 v[196:199], v207 offset:22528
	ds_read_b128 v[200:203], v207 offset:23552
	global_load_lds_dwordx4 v[204:205], off
	v_lshl_add_u64 v[204:205], s[48:49], 0, v[178:179]
	s_mov_b32 m0, s43
	s_addc_u32 s1, s49, 0
	global_load_lds_dwordx4 v[204:205], off
	v_lshl_add_u64 v[204:205], s[0:1], 0, v[174:175]
	s_mov_b32 m0, s53
	s_nop 0
	global_load_lds_dwordx4 v[204:205], off
	v_lshl_add_u64 v[204:205], s[0:1], 0, v[178:179]
	s_mov_b32 m0, s54
	s_nop 0
	global_load_lds_dwordx4 v[204:205], off
	v_lshl_add_u64 v[204:205], s[50:51], 0, v[172:173]
	s_mov_b32 m0, s56
	s_nop 0
	global_load_lds_dwordx4 v[204:205], off
	v_lshl_add_u64 v[204:205], s[50:51], 0, v[176:177]
	s_mov_b32 m0, s57
	s_nop 0
	global_load_lds_dwordx4 v[204:205], off
	s_waitcnt vmcnt(8)
	s_waitcnt lgkmcnt(0)
	s_barrier
	s_setprio 1
	s_waitcnt lgkmcnt(0)
	v_mfma_f32_16x16x32_bf16 v[60:63], v[72:75], v[160:163], 0
	v_mfma_f32_16x16x32_bf16 v[56:59], v[84:87], v[160:163], 0
	v_mfma_f32_16x16x32_bf16 v[44:47], v[72:75], v[168:171], 0
	v_mfma_f32_16x16x32_bf16 v[40:43], v[84:87], v[168:171], 0
	v_mfma_f32_16x16x32_bf16 v[28:31], v[72:75], v[188:191], 0
	v_mfma_f32_16x16x32_bf16 v[24:27], v[84:87], v[188:191], 0
	v_mfma_f32_16x16x32_bf16 v[12:15], v[72:75], v[196:199], 0
	v_mfma_f32_16x16x32_bf16 v[8:11], v[84:87], v[196:199], 0
	v_mfma_f32_16x16x32_bf16 v[60:63], v[76:79], v[164:167], v[60:63]
	v_mfma_f32_16x16x32_bf16 v[56:59], v[92:95], v[164:167], v[56:59]
	v_mfma_f32_16x16x32_bf16 v[44:47], v[76:79], v[184:187], v[44:47]
	v_mfma_f32_16x16x32_bf16 v[40:43], v[92:95], v[184:187], v[40:43]
	v_mfma_f32_16x16x32_bf16 v[28:31], v[76:79], v[192:195], v[28:31]
	v_mfma_f32_16x16x32_bf16 v[24:27], v[92:95], v[192:195], v[24:27]
	v_mfma_f32_16x16x32_bf16 v[12:15], v[76:79], v[200:203], v[12:15]
	v_mfma_f32_16x16x32_bf16 v[8:11], v[92:95], v[200:203], v[8:11]
	s_setprio 0
	s_setprio 1
	v_mfma_f32_16x16x32_bf16 v[52:55], v[144:147], v[160:163], 0
	v_mfma_f32_16x16x32_bf16 v[48:51], v[152:155], v[160:163], 0
	v_mfma_f32_16x16x32_bf16 v[36:39], v[144:147], v[168:171], 0
	v_mfma_f32_16x16x32_bf16 v[32:35], v[152:155], v[168:171], 0
	v_mfma_f32_16x16x32_bf16 v[20:23], v[144:147], v[188:191], 0
	v_mfma_f32_16x16x32_bf16 v[16:19], v[152:155], v[188:191], 0
	v_mfma_f32_16x16x32_bf16 v[4:7], v[144:147], v[196:199], 0
	v_mfma_f32_16x16x32_bf16 v[0:3], v[152:155], v[196:199], 0
	v_mfma_f32_16x16x32_bf16 v[52:55], v[148:151], v[164:167], v[52:55]
	v_mfma_f32_16x16x32_bf16 v[48:51], v[156:159], v[164:167], v[48:51]
	v_mfma_f32_16x16x32_bf16 v[36:39], v[148:151], v[184:187], v[36:39]
	v_mfma_f32_16x16x32_bf16 v[32:35], v[156:159], v[184:187], v[32:35]
	v_mfma_f32_16x16x32_bf16 v[20:23], v[148:151], v[192:195], v[20:23]
	v_mfma_f32_16x16x32_bf16 v[16:19], v[156:159], v[192:195], v[16:19]
	v_mfma_f32_16x16x32_bf16 v[4:7], v[148:151], v[200:203], v[4:7]
	v_mfma_f32_16x16x32_bf16 v[0:3], v[156:159], v[200:203], v[0:3]
	s_setprio 0
	s_barrier
	v_add_u32_e32 v92, s64, v206
	v_add_u32_e32 v156, s69, v206
	ds_read_b128 v[72:75], v92
	ds_read_b128 v[76:79], v92 offset:1024
	ds_read_b128 v[84:87], v92 offset:2048
	ds_read_b128 v[92:95], v92 offset:3072
	ds_read_b128 v[144:147], v156
	ds_read_b128 v[148:151], v156 offset:1024
	ds_read_b128 v[152:155], v156 offset:2048
	ds_read_b128 v[156:159], v156 offset:3072
	s_add_u32 s0, s50, 0x4000
	s_addc_u32 s1, s51, 0
	s_mov_b32 m0, s58
	v_lshl_add_u64 v[204:205], s[0:1], 0, v[172:173]
	ds_read_b128 v[160:163], v207 offset:32768
	ds_read_b128 v[164:167], v207 offset:33792
	ds_read_b128 v[168:171], v207 offset:34816
	ds_read_b128 v[184:187], v207 offset:35840
	ds_read_b128 v[188:191], v207 offset:36864
	ds_read_b128 v[192:195], v207 offset:37888
	ds_read_b128 v[196:199], v207 offset:38912
	ds_read_b128 v[200:203], v207 offset:39936
	global_load_lds_dwordx4 v[204:205], off
	v_lshl_add_u64 v[204:205], s[0:1], 0, v[176:177]
	s_mov_b32 m0, s59
	s_nop 0
	global_load_lds_dwordx4 v[204:205], off
	s_waitcnt vmcnt(8)
	s_waitcnt lgkmcnt(0)
	s_barrier
	s_setprio 1
	s_waitcnt lgkmcnt(0)
	v_mfma_f32_16x16x32_bf16 v[140:143], v[72:75], v[160:163], v[140:143]
	v_mfma_f32_16x16x32_bf16 v[136:139], v[84:87], v[160:163], v[136:139]
	v_mfma_f32_16x16x32_bf16 v[124:127], v[72:75], v[168:171], v[124:127]
	v_mfma_f32_16x16x32_bf16 v[120:123], v[84:87], v[168:171], v[120:123]
	v_mfma_f32_16x16x32_bf16 v[108:111], v[72:75], v[188:191], v[108:111]
	v_mfma_f32_16x16x32_bf16 v[104:107], v[84:87], v[188:191], v[104:107]
	v_mfma_f32_16x16x32_bf16 v[88:91], v[72:75], v[196:199], v[88:91]
	v_mfma_f32_16x16x32_bf16 v[80:83], v[84:87], v[196:199], v[80:83]
	v_mfma_f32_16x16x32_bf16 v[140:143], v[76:79], v[164:167], v[140:143]
	v_mfma_f32_16x16x32_bf16 v[136:139], v[92:95], v[164:167], v[136:139]
	v_mfma_f32_16x16x32_bf16 v[124:127], v[76:79], v[184:187], v[124:127]
	v_mfma_f32_16x16x32_bf16 v[120:123], v[92:95], v[184:187], v[120:123]
	v_mfma_f32_16x16x32_bf16 v[108:111], v[76:79], v[192:195], v[108:111]
	v_mfma_f32_16x16x32_bf16 v[104:107], v[92:95], v[192:195], v[104:107]
	v_mfma_f32_16x16x32_bf16 v[88:91], v[76:79], v[200:203], v[88:91]
	v_mfma_f32_16x16x32_bf16 v[80:83], v[92:95], v[200:203], v[80:83]
	s_setprio 0
	s_setprio 1
	v_mfma_f32_16x16x32_bf16 v[132:135], v[144:147], v[160:163], v[132:135]
	v_mfma_f32_16x16x32_bf16 v[128:131], v[152:155], v[160:163], v[128:131]
	v_mfma_f32_16x16x32_bf16 v[116:119], v[144:147], v[168:171], v[116:119]
	v_mfma_f32_16x16x32_bf16 v[112:115], v[152:155], v[168:171], v[112:115]
	v_mfma_f32_16x16x32_bf16 v[100:103], v[144:147], v[188:191], v[100:103]
	v_mfma_f32_16x16x32_bf16 v[96:99], v[152:155], v[188:191], v[96:99]
	v_mfma_f32_16x16x32_bf16 v[68:71], v[144:147], v[196:199], v[68:71]
	v_mfma_f32_16x16x32_bf16 v[64:67], v[152:155], v[196:199], v[64:67]
	v_mfma_f32_16x16x32_bf16 v[132:135], v[148:151], v[164:167], v[132:135]
	v_mfma_f32_16x16x32_bf16 v[128:131], v[156:159], v[164:167], v[128:131]
	v_mfma_f32_16x16x32_bf16 v[116:119], v[148:151], v[184:187], v[116:119]
	v_mfma_f32_16x16x32_bf16 v[112:115], v[156:159], v[184:187], v[112:115]
	v_mfma_f32_16x16x32_bf16 v[100:103], v[148:151], v[192:195], v[100:103]
	v_mfma_f32_16x16x32_bf16 v[96:99], v[156:159], v[192:195], v[96:99]
	v_mfma_f32_16x16x32_bf16 v[68:71], v[148:151], v[200:203], v[68:71]
	v_mfma_f32_16x16x32_bf16 v[64:67], v[156:159], v[200:203], v[64:67]
	s_setprio 0
	s_barrier
	s_add_u32 s0, s48, 0x8000
	s_addc_u32 s1, s49, 0
	s_mov_b32 m0, s65
	v_lshl_add_u64 v[204:205], s[0:1], 0, v[174:175]
	ds_read_b128 v[160:163], v207 offset:49152
	ds_read_b128 v[164:167], v207 offset:50176
	ds_read_b128 v[168:171], v207 offset:51200
	ds_read_b128 v[184:187], v207 offset:52224
	ds_read_b128 v[188:191], v207 offset:53248
	ds_read_b128 v[192:195], v207 offset:54272
	ds_read_b128 v[196:199], v207 offset:55296
	ds_read_b128 v[200:203], v207 offset:56320
	global_load_lds_dwordx4 v[204:205], off
	v_lshl_add_u64 v[204:205], s[0:1], 0, v[178:179]
	s_add_u32 s0, s48, 0xc000
	s_mov_b32 m0, s66
	s_addc_u32 s1, s49, 0
	global_load_lds_dwordx4 v[204:205], off
	v_lshl_add_u64 v[204:205], s[0:1], 0, v[174:175]
	s_mov_b32 m0, s70
	s_nop 0
	global_load_lds_dwordx4 v[204:205], off
	v_lshl_add_u64 v[204:205], s[0:1], 0, v[178:179]
	s_mov_b32 m0, s71
	s_nop 0
	global_load_lds_dwordx4 v[204:205], off
	v_lshl_add_u64 v[204:205], s[46:47], 0, v[172:173]
	s_mov_b32 m0, s67
	s_nop 0
	global_load_lds_dwordx4 v[204:205], off
	v_lshl_add_u64 v[204:205], s[46:47], 0, v[176:177]
	s_mov_b32 m0, s68
	s_nop 0
	global_load_lds_dwordx4 v[204:205], off
	s_waitcnt vmcnt(8)
	s_waitcnt lgkmcnt(0)
	s_barrier
	s_setprio 1
	s_waitcnt lgkmcnt(0)
	v_mfma_f32_16x16x32_bf16 v[60:63], v[72:75], v[160:163], v[60:63]
	v_mfma_f32_16x16x32_bf16 v[56:59], v[84:87], v[160:163], v[56:59]
	v_mfma_f32_16x16x32_bf16 v[44:47], v[72:75], v[168:171], v[44:47]
	v_mfma_f32_16x16x32_bf16 v[40:43], v[84:87], v[168:171], v[40:43]
	v_mfma_f32_16x16x32_bf16 v[28:31], v[72:75], v[188:191], v[28:31]
	v_mfma_f32_16x16x32_bf16 v[24:27], v[84:87], v[188:191], v[24:27]
	v_mfma_f32_16x16x32_bf16 v[12:15], v[72:75], v[196:199], v[12:15]
	v_mfma_f32_16x16x32_bf16 v[8:11], v[84:87], v[196:199], v[8:11]
	v_mfma_f32_16x16x32_bf16 v[60:63], v[76:79], v[164:167], v[60:63]
	v_mfma_f32_16x16x32_bf16 v[56:59], v[92:95], v[164:167], v[56:59]
	v_mfma_f32_16x16x32_bf16 v[44:47], v[76:79], v[184:187], v[44:47]
	v_mfma_f32_16x16x32_bf16 v[40:43], v[92:95], v[184:187], v[40:43]
	v_mfma_f32_16x16x32_bf16 v[28:31], v[76:79], v[192:195], v[28:31]
	v_mfma_f32_16x16x32_bf16 v[24:27], v[92:95], v[192:195], v[24:27]
	v_mfma_f32_16x16x32_bf16 v[12:15], v[76:79], v[200:203], v[12:15]
	v_mfma_f32_16x16x32_bf16 v[8:11], v[92:95], v[200:203], v[8:11]
	s_setprio 0
	s_setprio 1
	v_mfma_f32_16x16x32_bf16 v[52:55], v[144:147], v[160:163], v[52:55]
	v_mfma_f32_16x16x32_bf16 v[48:51], v[152:155], v[160:163], v[48:51]
	v_mfma_f32_16x16x32_bf16 v[36:39], v[144:147], v[168:171], v[36:39]
	v_mfma_f32_16x16x32_bf16 v[32:35], v[152:155], v[168:171], v[32:35]
	v_mfma_f32_16x16x32_bf16 v[20:23], v[144:147], v[188:191], v[20:23]
	v_mfma_f32_16x16x32_bf16 v[16:19], v[152:155], v[188:191], v[16:19]
	v_mfma_f32_16x16x32_bf16 v[4:7], v[144:147], v[196:199], v[4:7]
	v_mfma_f32_16x16x32_bf16 v[0:3], v[152:155], v[196:199], v[0:3]
	v_mfma_f32_16x16x32_bf16 v[52:55], v[148:151], v[164:167], v[52:55]
	v_mfma_f32_16x16x32_bf16 v[48:51], v[156:159], v[164:167], v[48:51]
	v_mfma_f32_16x16x32_bf16 v[36:39], v[148:151], v[184:187], v[36:39]
	v_mfma_f32_16x16x32_bf16 v[32:35], v[156:159], v[184:187], v[32:35]
	v_mfma_f32_16x16x32_bf16 v[20:23], v[148:151], v[192:195], v[20:23]
	v_mfma_f32_16x16x32_bf16 v[16:19], v[156:159], v[192:195], v[16:19]
	v_mfma_f32_16x16x32_bf16 v[4:7], v[148:151], v[200:203], v[4:7]
	v_mfma_f32_16x16x32_bf16 v[0:3], v[156:159], v[200:203], v[0:3]
	s_setprio 0
	s_barrier
	s_add_i32 s76, s76, 2
	s_add_u32 s74, s74, 0x10000
	s_addc_u32 s75, s75, 0
	s_cmpk_gt_u32 s76, 0x7d
	s_mov_b64 s[0:1], s[44:45]
	.p2align	6
